# scan compute waves: B2 barrier moved up to the last LDS read of the chunk (h normalisation + stores now overlap the loader's commit)
# speedup vs baseline: 1.0173x; 1.0035x over previous
; #define LAS __attribute__((address_space(3)))
; __device__ __forceinline__ void p4_scan(const Args& a, const Frame& F) {
;     ...
;                     const float denA = __shfl(acc2A[2][0] + decA * acc3A[2][0], c), denB = __shfl(acc2B[2][0] + decB * acc3B[2][0], c);
;                     const float invA = frcp_(fmaxf(fabsf(denA), emtA)), invB = frcp_(fmaxf(fabsf(denB), emtB));
;                     { bf16* HXs = store ? HX : (bf16*)(a.ws + WS_H2) - (size_t)T * 512;
;                         const int lnh = c + 16 * q, pfh = (lnh >> 2) & 15, pqh = lnh & 3, bah = 4 * (pfh + 16 * pqh);
;                         const int tokA = base + (dir ? 127 - (16 * ta + pfh) : (16 * ta + pfh)), tokB = base + (dir ? 127 - (16 * tb + pfh) : (16 * tb + pfh));
; #pragma unroll
;                         for (int mt = 0; mt < 2; ++mt) { const f32x4 vA = (acc2A[mt] + acc3A[mt] * decA) * invA, vB = (acc2B[mt] + acc3B[mt] * decB) * invB;
;                             u32x2 o; o.x = pg8::cvt_pk_bf16(vA[0], vA[1]); o.y = pg8::cvt_pk_bf16(vA[2], vA[3]);
;                             o.x = (unsigned)__builtin_amdgcn_ds_bpermute(bah, (int)o.x); o.y = (unsigned)__builtin_amdgcn_ds_bpermute(bah, (int)o.y);
;                             *(u32x2*)(HXs + (size_t)tokA * 512 + h * 128 + vs * 32 + 16 * mt + 4 * pqh) = o;
;                             o.x = pg8::cvt_pk_bf16(vB[0], vB[1]); o.y = pg8::cvt_pk_bf16(vB[2], vB[3]);
;                             o.x = (unsigned)__builtin_amdgcn_ds_bpermute(bah, (int)o.x); o.y = (unsigned)__builtin_amdgcn_ds_bpermute(bah, (int)o.y);
;                             *(u32x2*)(HXs + (size_t)tokB * 512 + h * 128 + vs * 32 + 16 * mt + 4 * pqh) = o; } }
;                 }
;                 LDS_BARRIER();
;                 {
;                     bf16x8 vf[3][4];
; #pragma unroll
;                     for (int nt = 0; nt < 3; ++nt)
; #pragma unroll
;                         for (int ks = 0; ks < 4; ++ks) vf[nt][ks] = *(const LAS bf16x8*)(L + vacur + (16 * nt + c) * SP + (ks * 32 + q * 8) * 2);
; #pragma unroll
;                     for (int d2 = 0; d2 < 2; ++d2) {
;                         unsigned ka[8];
; #pragma unroll
;                         for (int i = 0; i < 8; ++i) ka[i] = Lb + (unsigned)kcur + kadA[i] + (d2 ? 32u : 0u);
;                         u32x2 kr[8]; tr_read_k8(kr, ka);
; #pragma unroll
.LBB0_449:
	v_max_f32_e32 v49, v153, v153
	v_max_f32_e32 v49, v49, v205
	v_sub_f32_e32 v50, v201, v49
	v_mul_f32_e32 v50, 0x3fb8aa3b, v50
	v_exp_f32_e32 v72, v50
	s_waitcnt lgkmcnt(1)
	v_add_f32_e32 v50, v204, v203
	v_add_f32_e32 v71, v152, v49
	v_sub_f32_e32 v49, v201, v204
	v_mul_f32_e32 v51, 0xbfb8aa3b, v50
	v_sub_f32_e32 v50, v201, v53
	v_mul_f32_e32 v49, 0x3fb8aa3b, v49
	v_mul_f32_e32 v73, 0x3fb8aa3b, v50
	s_waitcnt lgkmcnt(0)
	s_barrier
	v_add_f32_e32 v50, v53, v202
	v_mul_f32_e32 v53, 0xbfb8aa3b, v50
	v_exp_f32_e32 v50, v49
	v_exp_f32_e32 v76, v73
	v_exp_f32_e32 v49, v51
	v_exp_f32_e32 v51, v53
	v_fmac_f32_e32 v70, v52, v50
	ds_bpermute_b32 v52, v200, v70
	v_fmac_f32_e32 v74, v48, v76
	ds_bpermute_b32 v53, v200, v74
	s_and_b64 s[6:7], s[50:51], exec
	s_cselect_b32 s6, s92, 0x1de20
	s_waitcnt lgkmcnt(1)
	v_max_f32_e64 v48, |v52|, |v52|
	v_max_f32_e32 v48, v48, v49
	v_rcp_f32_e32 v48, v48
	s_waitcnt lgkmcnt(0)
	v_max_f32_e64 v49, |v53|, |v53|
	s_cmp_gt_u32 s11, 1
	v_max_f32_e32 v49, v49, v51
	v_pk_fma_f32 v[44:45], v[44:45], v[50:51], v[66:67] op_sel_hi:[1,0,1]
	s_cselect_b32 s8, s77, 0x23200000
	v_add_u32_e32 v74, s64, v186
	v_pk_fma_f32 v[46:47], v[46:47], v[50:51], v[68:69] op_sel_hi:[1,0,1]
	v_pk_mul_f32 v[44:45], v[44:45], v[48:49] op_sel_hi:[1,0]
	s_cselect_b32 s7, 0, 0
	s_add_u32 s8, s72, s8
	v_ashrrev_i32_e32 v75, 31, v74
	v_pk_mul_f32 v[46:47], v[46:47], v[48:49] op_sel_hi:[1,0]
	v_cvt_pk_bf16_f32 v44, v44, v45
	v_rcp_f32_e32 v52, v49
	v_cvt_pk_bf16_f32 v45, v46, v47
	s_addc_u32 s9, s73, s7
	v_lshlrev_b64 v[74:75], 10, v[74:75]
	ds_bpermute_b32 v44, v185, v44
	ds_bpermute_b32 v45, v185, v45
	v_lshl_add_u64 v[74:75], s[8:9], 0, v[74:75]
	v_lshl_add_u64 v[74:75], v[74:75], 0, s[44:45]
	s_mov_b32 s11, s45
	v_lshl_add_u64 v[74:75], v[74:75], 0, s[10:11]
	v_pk_fma_f32 v[40:41], v[40:41], v[76:77], v[62:63] op_sel_hi:[1,0,1]
	v_add_u32_e32 v78, s64, v187
	v_lshl_add_u64 v[74:75], v[74:75], 0, v[144:145]
	v_pk_fma_f32 v[42:43], v[42:43], v[76:77], v[64:65] op_sel_hi:[1,0,1]
	v_pk_mul_f32 v[40:41], v[40:41], v[52:53] op_sel_hi:[1,0]
	v_ashrrev_i32_e32 v79, 31, v78
	v_pk_mul_f32 v[42:43], v[42:43], v[52:53] op_sel_hi:[1,0]
	s_waitcnt lgkmcnt(0)
	global_store_dwordx2 v[74:75], v[44:45], off
	v_cvt_pk_bf16_f32 v40, v40, v41
	v_cvt_pk_bf16_f32 v41, v42, v43
	v_lshlrev_b64 v[78:79], 10, v[78:79]
	ds_bpermute_b32 v40, v185, v40
	ds_bpermute_b32 v41, v185, v41
	v_lshl_add_u64 v[78:79], s[8:9], 0, v[78:79]
	v_lshl_add_u64 v[78:79], v[78:79], 0, s[44:45]
	v_lshl_add_u64 v[78:79], v[78:79], 0, s[10:11]
	v_pk_fma_f32 v[36:37], v[36:37], v[50:51], v[58:59] op_sel_hi:[1,0,1]
	v_lshl_add_u64 v[78:79], v[78:79], 0, v[144:145]
	v_pk_fma_f32 v[38:39], v[38:39], v[50:51], v[60:61] op_sel_hi:[1,0,1]
	v_pk_mul_f32 v[36:37], v[36:37], v[48:49] op_sel_hi:[1,0]
	s_waitcnt lgkmcnt(0)
	global_store_dwordx2 v[78:79], v[40:41], off
	v_pk_mul_f32 v[38:39], v[38:39], v[48:49] op_sel_hi:[1,0]
	v_cvt_pk_bf16_f32 v36, v36, v37
	ds_bpermute_b32 v36, v185, v36
	v_cvt_pk_bf16_f32 v37, v38, v39
	ds_bpermute_b32 v37, v185, v37
	v_pk_fma_f32 v[32:33], v[32:33], v[76:77], v[54:55] op_sel_hi:[1,0,1]
	v_pk_fma_f32 v[34:35], v[34:35], v[76:77], v[56:57] op_sel_hi:[1,0,1]
	v_pk_mul_f32 v[32:33], v[32:33], v[52:53] op_sel_hi:[1,0]
	v_pk_mul_f32 v[34:35], v[34:35], v[52:53] op_sel_hi:[1,0]
	s_waitcnt lgkmcnt(0)
	global_store_dwordx2 v[74:75], v[36:37], off offset:32
	v_cvt_pk_bf16_f32 v32, v32, v33
	v_cvt_pk_bf16_f32 v33, v34, v35
	ds_bpermute_b32 v32, v185, v32
	ds_bpermute_b32 v33, v185, v33
	v_add_u32_e32 v36, s6, v189
	s_add_i32 s6, s35, 0
	v_add_u32_e32 v73, s6, v172
	v_pk_mul_f32 v[10:11], v[10:11], v[72:73] op_sel_hi:[1,0]
	s_waitcnt lgkmcnt(0)
	global_store_dwordx2 v[78:79], v[32:33], off offset:32
	s_waitcnt lgkmcnt(0)
	v_pk_mul_f32 v[8:9], v[8:9], v[72:73] op_sel_hi:[1,0]
	ds_read_b128 v[52:55], v36
	ds_read_b128 v[56:59], v36 offset:64
	ds_read_b128 v[44:47], v36 offset:128
	ds_read_b128 v[32:35], v36 offset:192
	ds_read_b128 v[60:63], v36 offset:4352
	ds_read_b128 v[64:67], v36 offset:4416
	ds_read_b128 v[48:51], v36 offset:4480
	ds_read_b128 v[40:43], v36 offset:4544
	ds_read_b128 v[74:77], v36 offset:8704
	ds_read_b128 v[78:81], v36 offset:8768
	ds_read_b128 v[82:85], v36 offset:8832
	ds_read_b128 v[36:39], v36 offset:8896
	v_add_u32_e32 v68, s6, v148
	v_add_u32_e32 v69, s6, v149
	v_add_u32_e32 v70, s6, v171
	v_add_u32_e32 v102, s6, v173
	v_add_u32_e32 v103, s6, v174
	v_add_u32_e32 v104, s6, v175
	v_add_u32_e32 v105, s6, v176
	ds_read_b64_tr_b16 v[98:99], v68
	ds_read_b64_tr_b16 v[100:101], v69
	ds_read_b64_tr_b16 v[94:95], v70
	ds_read_b64_tr_b16 v[96:97], v73
	ds_read_b64_tr_b16 v[90:91], v102
	ds_read_b64_tr_b16 v[92:93], v103
	ds_read_b64_tr_b16 v[86:87], v104
	ds_read_b64_tr_b16 v[88:89], v105
	s_waitcnt lgkmcnt(0)
	v_pk_mul_f32 v[14:15], v[14:15], v[72:73] op_sel_hi:[1,0]
	s_waitcnt lgkmcnt(11)
	v_mfma_f32_16x16x32_bf16 v[8:11], v[98:101], v[52:55], v[8:11]
	v_mul_f32_e64 v12, v12, v72
	v_mul_f32_e64 v13, v13, v72
	v_pk_mul_f32 v[18:19], v[18:19], v[72:73] op_sel_hi:[1,0]
	v_pk_mul_f32 v[16:17], v[16:17], v[72:73] op_sel_hi:[1,0]
	s_waitcnt lgkmcnt(10)
; #define LAS __attribute__((address_space(3)))
; __device__ __forceinline__ unsigned pk2(float lo, float hi) { return f2bf(lo) | (f2bf(hi) << 16); }
; #define LDS_BARRIER() do { asm volatile("s_waitcnt lgkmcnt(0)" ::: "memory"); __builtin_amdgcn_s_barrier(); asm volatile("" ::: "memory"); } while (0)
; __device__ __forceinline__ void p4_scan(const Args& a, const Frame& F) {
;     ...
; #pragma unroll
;                     for (int d2 = 0; d2 < 2; ++d2) {
;                         unsigned ka[8];
; #pragma unroll
;                         for (int i = 0; i < 8; ++i) ka[i] = Lb + (unsigned)kcur + kadA[i] + (d2 ? 32u : 0u);
;                         u32x2 kr[8]; tr_read_k8(kr, ka);
; #pragma unroll
;                         for (int nt = 0; nt < 3; ++nt) accC[d2][nt] = accC[d2][nt] * cd;
; #pragma unroll
;                         for (int ks = 0; ks < 4; ++ks) { const bf16x8 af = mk_frag(kr[ks * 2], kr[ks * 2 + 1]);
; #pragma unroll
;                             for (int nt = 0; nt < 3; ++nt) accC[d2][nt] = __builtin_amdgcn_mfma_f32_16x16x32_bf16(af, vf[nt][ks], accC[d2][nt], 0, 0, 0); }
; #pragma unroll
;                         for (int nt = 0; nt < 3; ++nt) { u32x2 o; o.x = pk2(accC[d2][nt][0], accC[d2][nt][1]); o.y = pk2(accC[d2][nt][2], accC[d2][nt][3]);
;                             *(LAS u32x2*)(L + S_CT + (16 * nt + c) * SP + (16 * (2 * w + d2) + 4 * q) * 2) = o; }
;                     }
;                 }
;                 mcar = mnew;
;                 btot = pbt; pmx = ppx;
;                 LDS_BARRIER();
	v_mfma_f32_16x16x32_bf16 v[8:11], v[94:97], v[56:59], v[8:11]
	s_add_i32 s6, s6, 32
	v_add_u32_e32 v73, s6, v172
	v_pk_mul_f32 v[22:23], v[22:23], v[72:73] op_sel_hi:[1,0]
	s_waitcnt lgkmcnt(7)
	v_mfma_f32_16x16x32_bf16 v[12:15], v[98:101], v[60:63], v[12:15]
	v_mul_f32_e64 v20, v20, v72
	v_mul_f32_e64 v21, v21, v72
	v_add_u32_e32 v102, s6, v173
	v_add_u32_e32 v103, s6, v174
	v_mfma_f32_16x16x32_bf16 v[8:11], v[90:93], v[44:47], v[8:11]
	v_add_u32_e32 v104, s6, v175
	v_add_u32_e32 v105, s6, v176
	v_pk_mul_f32 v[26:27], v[26:27], v[72:73] op_sel_hi:[1,0]
	s_waitcnt lgkmcnt(6)
	v_mfma_f32_16x16x32_bf16 v[12:15], v[94:97], v[64:67], v[12:15]
	v_mul_f32_e64 v24, v24, v72
	v_mul_f32_e64 v25, v25, v72
	v_pk_mul_f32 v[30:31], v[30:31], v[72:73] op_sel_hi:[1,0]
	v_pk_mul_f32 v[28:29], v[28:29], v[72:73] op_sel_hi:[1,0]
	v_mfma_f32_16x16x32_bf16 v[8:11], v[86:89], v[32:35], v[8:11]
	s_cmpk_eq_i32 s34, 0x42
	v_mov_b32_e32 v201, v71
	s_mov_b32 s11, s34
	s_waitcnt lgkmcnt(3)
	v_mfma_f32_16x16x32_bf16 v[16:19], v[98:101], v[74:77], v[16:19]
	s_waitcnt vmcnt(4)
	v_mov_b64_e32 v[152:153], v[150:151]
	s_nop 0
	v_bfe_u32 v68, v8, 16, 1
	v_add3_u32 v68, v8, v68, s93
	v_mfma_f32_16x16x32_bf16 v[12:15], v[90:93], v[48:51], v[12:15]
	v_bfe_u32 v69, v9, 16, 1
	v_lshrrev_b32_e32 v68, 16, v68
	v_add3_u32 v69, v9, v69, s93
	s_waitcnt lgkmcnt(2)
	v_mfma_f32_16x16x32_bf16 v[16:19], v[94:97], v[78:81], v[16:19]
	v_and_or_b32 v68, v69, s94, v68
	v_bfe_u32 v69, v10, 16, 1
	v_add3_u32 v69, v10, v69, s93
	v_mfma_f32_16x16x32_bf16 v[12:15], v[86:89], v[40:43], v[12:15]
	v_bfe_u32 v70, v11, 16, 1
	v_lshrrev_b32_e32 v69, 16, v69
	v_add3_u32 v70, v11, v70, s93
	s_waitcnt lgkmcnt(1)
	v_mfma_f32_16x16x32_bf16 v[16:19], v[90:93], v[82:85], v[16:19]
	v_and_or_b32 v69, v70, s94, v69
	ds_write_b64 v197, v[68:69]
	s_nop 0
	v_bfe_u32 v68, v12, 16, 1
	v_add3_u32 v68, v12, v68, s93
	v_bfe_u32 v69, v13, 16, 1
	v_lshrrev_b32_e32 v68, 16, v68
	v_add3_u32 v69, v13, v69, s93
	s_waitcnt lgkmcnt(1)
	v_mfma_f32_16x16x32_bf16 v[16:19], v[86:89], v[36:39], v[16:19]
	v_and_or_b32 v68, v69, s94, v68
	v_bfe_u32 v69, v14, 16, 1
	v_add3_u32 v69, v14, v69, s93
	v_bfe_u32 v70, v15, 16, 1
	v_lshrrev_b32_e32 v69, 16, v69
	v_add3_u32 v70, v15, v70, s93
	v_and_or_b32 v69, v70, s94, v69
	ds_write_b64 v197, v[68:69] offset:4352
	v_bfe_u32 v68, v16, 16, 1
	v_add3_u32 v68, v16, v68, s93
	v_bfe_u32 v69, v17, 16, 1
	v_lshrrev_b32_e32 v68, 16, v68
	v_add3_u32 v69, v17, v69, s93
	v_and_or_b32 v68, v69, s94, v68
	v_bfe_u32 v69, v18, 16, 1
	v_add3_u32 v69, v18, v69, s93
	v_bfe_u32 v70, v19, 16, 1
	v_lshrrev_b32_e32 v69, 16, v69
	v_add3_u32 v70, v19, v70, s93
	v_and_or_b32 v69, v70, s94, v69
	ds_write_b64 v197, v[68:69] offset:8704
	v_add_u32_e32 v68, s6, v148
	v_add_u32_e32 v69, s6, v149
	v_add_u32_e32 v70, s6, v171
	ds_read_b64_tr_b16 v[98:99], v68
	ds_read_b64_tr_b16 v[100:101], v69
	ds_read_b64_tr_b16 v[94:95], v70
	ds_read_b64_tr_b16 v[96:97], v73
	ds_read_b64_tr_b16 v[90:91], v102
	ds_read_b64_tr_b16 v[92:93], v103
	ds_read_b64_tr_b16 v[86:87], v104
	ds_read_b64_tr_b16 v[88:89], v105
	s_waitcnt lgkmcnt(0)
	s_nop 0
	v_mfma_f32_16x16x32_bf16 v[20:23], v[98:101], v[52:55], v[20:23]
	v_mfma_f32_16x16x32_bf16 v[20:23], v[94:97], v[56:59], v[20:23]
	v_mfma_f32_16x16x32_bf16 v[24:27], v[98:101], v[60:63], v[24:27]
	v_mfma_f32_16x16x32_bf16 v[20:23], v[90:93], v[44:47], v[20:23]
	v_mfma_f32_16x16x32_bf16 v[24:27], v[94:97], v[64:67], v[24:27]
	v_mfma_f32_16x16x32_bf16 v[20:23], v[86:89], v[32:35], v[20:23]
	v_mfma_f32_16x16x32_bf16 v[28:31], v[98:101], v[74:77], v[28:31]
	v_mfma_f32_16x16x32_bf16 v[24:27], v[90:93], v[48:51], v[24:27]
	s_nop 5
	v_bfe_u32 v32, v20, 16, 1
	v_add3_u32 v32, v20, v32, s93
	v_bfe_u32 v33, v21, 16, 1
	v_mfma_f32_16x16x32_bf16 v[28:31], v[94:97], v[78:81], v[28:31]
	v_lshrrev_b32_e32 v32, 16, v32
	v_add3_u32 v33, v21, v33, s93
	v_and_or_b32 v32, v33, s94, v32
	v_mfma_f32_16x16x32_bf16 v[24:27], v[86:89], v[40:43], v[24:27]
	v_bfe_u32 v33, v22, 16, 1
	v_add3_u32 v33, v22, v33, s93
	v_bfe_u32 v34, v23, 16, 1
	v_lshrrev_b32_e32 v33, 16, v33
	v_add3_u32 v34, v23, v34, s93
	v_mfma_f32_16x16x32_bf16 v[28:31], v[90:93], v[82:85], v[28:31]
	v_and_or_b32 v33, v34, s94, v33
	ds_write_b64 v197, v[32:33] offset:32
	v_bfe_u32 v32, v24, 16, 1
	v_add3_u32 v32, v24, v32, s93
	v_bfe_u32 v33, v25, 16, 1
	v_lshrrev_b32_e32 v32, 16, v32
	v_add3_u32 v33, v25, v33, s93
	v_mfma_f32_16x16x32_bf16 v[28:31], v[86:89], v[36:39], v[28:31]
	v_and_or_b32 v32, v33, s94, v32
	v_bfe_u32 v33, v26, 16, 1
	v_add3_u32 v33, v26, v33, s93
	v_bfe_u32 v34, v27, 16, 1
	v_lshrrev_b32_e32 v33, 16, v33
	v_add3_u32 v34, v27, v34, s93
	v_and_or_b32 v33, v34, s94, v33
	ds_write_b64 v197, v[32:33] offset:4384
	v_bfe_u32 v32, v28, 16, 1
	v_add3_u32 v32, v28, v32, s93
	v_bfe_u32 v33, v29, 16, 1
	v_lshrrev_b32_e32 v32, 16, v32
	v_add3_u32 v33, v29, v33, s93
	v_and_or_b32 v32, v33, s94, v32
	v_bfe_u32 v33, v30, 16, 1
	v_add3_u32 v33, v30, v33, s93
	v_bfe_u32 v34, v31, 16, 1
	v_lshrrev_b32_e32 v33, 16, v33
	v_add3_u32 v34, v31, v34, s93
	v_and_or_b32 v33, v34, s94, v33
	ds_write_b64 v197, v[32:33] offset:8736
	s_waitcnt lgkmcnt(0)
	s_barrier
	s_cbranch_scc1 .LBB0_472
